# work-queue steal scan (P3/P4/P19/P12/P13): the up-to-7 serialized device-scope counter polls at queue exhaustion replaced by one 8-lane snapshot load read back with v_readlane
# speedup vs baseline: 1.0005x; 1.0005x over previous
; #define LAS __attribute__((address_space(3)))
; __device__ __forceinline__ int lane_id_v() { int l; asm volatile("v_mbcnt_lo_u32_b32 %0, -1, 0\n\tv_mbcnt_hi_u32_b32 %0, -1, %0" : "=v"(l)); return l & 63; }
; __device__ __forceinline__ int opaque_i(int x) { asm volatile("" : "+v"(x)); return x; }
; __device__ __forceinline__ int next_unit_pre(QPre& qp, unsigned* counters, int per_queue, LAS unsigned char* lds, int slot_off, const int wave) {
;     volatile LAS int* slot = (volatile LAS int*)(lds + opaque_i(slot_off));
;     const unsigned x = ((unsigned)__builtin_amdgcn_s_getreg((3 << 11) | 20)) & 7u;
;     qp.ctr = counters + x * 64;
;     if (wave == 0 && lane_id_v() == 0) {
;         int res = -1;
;         unsigned k0 = 0u;
;         if (qp.issued) { if (qp.pre < (unsigned)per_queue) res = (int)(x * (unsigned)per_queue + qp.pre); k0 = 1u; }
;         if (res < 0) {
;             for (unsigned k = k0; k < 8u; ++k) {
;                 const unsigned q = (x + k) & 7u;
;                 if (k > 0 && __hip_atomic_load(counters + q * 64, __ATOMIC_RELAXED, __HIP_MEMORY_SCOPE_AGENT) >= (unsigned)per_queue) continue;
;                 const unsigned idx = __hip_atomic_fetch_add(counters + q * 64, 1u, __ATOMIC_RELAXED, __HIP_MEMORY_SCOPE_AGENT);
;                 if (idx < (unsigned)per_queue) { res = (int)(q * (unsigned)per_queue + idx); break; }
;             }
;         }
;         slot[0] = res;
.LBB0_616:
	s_nop 1
	v_mov_b32_e32 v0, 0x1fc00
	v_readlane_b32 s2, v254, 26
	s_getreg_b32 s1, hwreg(HW_REG_XCC_ID, 0, 4)
	v_readlane_b32 s3, v254, 27
	s_and_b64 vcc, exec, s[2:3]
	s_and_b32 s0, s1, 7
	s_cbranch_vccnz .LBB0_632
	v_mbcnt_lo_u32_b32 v1, -1, 0
	v_mbcnt_hi_u32_b32 v1, -1, v1
	s_nop 0
	v_and_b32_e32 v1, 63, v1
	v_cmp_eq_u32_e32 vcc, 0, v1
	s_and_saveexec_b64 s[4:5], vcc
	s_cbranch_execz .LBB0_631
	v_and_b32_e32 v1, 1, v103
	v_cmp_eq_u32_e32 vcc, 1, v1
	s_movk_i32 s2, 0xff
	v_cmp_lt_u32_e64 s[2:3], s2, v93
	v_lshl_add_u32 v1, s0, 8, v93
	s_xor_b64 s[6:7], vcc, -1
	s_or_b64 s[2:3], s[6:7], s[2:3]
	v_cmp_gt_i32_e32 vcc, 0, v1
	s_or_b64 s[6:7], s[2:3], vcc
	s_and_saveexec_b64 s[2:3], s[6:7]
	s_cbranch_execz .LBB0_630
	v_and_b32_e32 v2, 0xff, v103
	v_mov_b32_e32 v1, -1
	s_mov_b64 s[6:7], 0
	s_mov_b64 s[98:99], exec
	s_mov_b64 exec, 0xff
	v_mbcnt_lo_u32_b32 v176, -1, 0
	v_lshlrev_b32_e32 v176, 8, v176
	global_load_dword v176, v176, s[40:41] sc1
	s_waitcnt vmcnt(0)
	s_mov_b64 exec, s[98:99]
	s_branch .LBB0_621

; __device__ __forceinline__ int next_unit_pre(QPre& qp, unsigned* counters, int per_queue, LAS unsigned char* lds, int slot_off, const int wave) {
;     ...
;             for (unsigned k = k0; k < 8u; ++k) {
;                 const unsigned q = (x + k) & 7u;
;                 if (k > 0 && __hip_atomic_load(counters + q * 64, __ATOMIC_RELAXED, __HIP_MEMORY_SCOPE_AGENT) >= (unsigned)per_queue) continue;
;                 const unsigned idx = __hip_atomic_fetch_add(counters + q * 64, 1u, __ATOMIC_RELAXED, __HIP_MEMORY_SCOPE_AGENT);
;                 if (idx < (unsigned)per_queue) { res = (int)(q * (unsigned)per_queue + idx); break; }
.LBB0_621:
	v_add_u32_e32 v3, s1, v2
	v_and_b32_e32 v3, 7, v3
	v_lshlrev_b32_e32 v4, 6, v3
	v_cmp_eq_u32_e64 s[8:9], 0, v2
	v_cmp_ne_u32_e32 vcc, 0, v2
	v_lshlrev_b32_e32 v4, 2, v4
	s_and_saveexec_b64 s[10:11], vcc
	s_cbranch_execz .LBB0_623
	v_readfirstlane_b32 s101, v3
	s_nop 3
	v_readlane_b32 s100, v176, s101
	s_nop 1
	v_mov_b32_e32 v5, s100
	s_andn2_b64 s[8:9], s[8:9], exec
	v_cmp_gt_u32_e32 vcc, s95, v5
	s_and_b64 s[12:13], vcc, exec
	s_or_b64 s[8:9], s[8:9], s[12:13]

; __device__ __forceinline__ int next_unit(unsigned* counters, int per_queue, LAS unsigned char* lds, int slot_off, const int wave) {
;     ...
;         for (unsigned k = 0; k < 8u; ++k) {
;             const unsigned q = (x + k) & 7u;
;             if (k > 0 && __hip_atomic_load(counters + q * 64, __ATOMIC_RELAXED, __HIP_MEMORY_SCOPE_AGENT) >= (unsigned)per_queue) continue;
;             const unsigned idx = __hip_atomic_fetch_add(counters + q * 64, 1u, __ATOMIC_RELAXED, __HIP_MEMORY_SCOPE_AGENT);
;             if (idx < (unsigned)per_queue) { res = (int)(q * (unsigned)per_queue + idx); break; }
;         }
;         slot[0] = res;
.LBB0_720:
	s_or_b64 exec, exec, s[6:7]
	s_waitcnt vmcnt(0)
	v_readfirstlane_b32 s4, v1
	s_nop 1
	v_add_u32_e32 v0, s4, v0
	v_cmp_lt_u32_e32 vcc, s89, v0
	v_lshl_add_u32 v0, s1, 8, v0
	s_and_saveexec_b64 s[4:5], vcc
	s_cbranch_execz .LBB0_773
	s_mov_b64 s[98:99], exec
	s_mov_b64 exec, 0xff
	v_mbcnt_lo_u32_b32 v140, -1, 0
	v_lshlrev_b32_e32 v140, 8, v140
	global_load_dword v140, v140, s[38:39] sc1
	s_waitcnt vmcnt(0)
	s_mov_b64 exec, s[98:99]
	s_add_i32 s6, s0, 1
	s_and_b32 s12, s6, 7
	s_lshl_b32 s6, s12, 8
	v_mov_b32_e32 v0, s6
	v_readlane_b32 s100, v140, s12
	s_nop 1
	v_mov_b32_e32 v0, s100
	s_add_u32 s6, s38, s6
	s_addc_u32 s7, s39, 0
	v_cmp_lt_u32_e32 vcc, s89, v0
	s_cbranch_vccnz .LBB0_725
	s_mov_b64 s[10:11], exec
	v_mbcnt_lo_u32_b32 v0, s10, 0
	v_mbcnt_hi_u32_b32 v0, s11, v0
	v_cmp_eq_u32_e32 vcc, 0, v0
	s_and_saveexec_b64 s[8:9], vcc
	s_cbranch_execz .LBB0_724
	s_bcnt1_i32_b64 s10, s[10:11]
	v_mov_b32_e32 v1, s10
	global_atomic_add v1, v177, v1, s[6:7] sc0

; __device__ __forceinline__ int next_unit(unsigned* counters, int per_queue, LAS unsigned char* lds, int slot_off, const int wave) {
;     ...
;         for (unsigned k = 0; k < 8u; ++k) {
;             const unsigned q = (x + k) & 7u;
;             if (k > 0 && __hip_atomic_load(counters + q * 64, __ATOMIC_RELAXED, __HIP_MEMORY_SCOPE_AGENT) >= (unsigned)per_queue) continue;
;             const unsigned idx = __hip_atomic_fetch_add(counters + q * 64, 1u, __ATOMIC_RELAXED, __HIP_MEMORY_SCOPE_AGENT);
;             if (idx < (unsigned)per_queue) { res = (int)(q * (unsigned)per_queue + idx); break; }
;         }
;         slot[0] = res;
.LBB0_727:
	s_or_b64 exec, exec, s[6:7]
	s_and_saveexec_b64 s[6:7], s[8:9]
	s_cbranch_execz .LBB0_772
	s_add_i32 s8, s0, 2
	s_and_b32 s14, s8, 7
	s_lshl_b32 s8, s14, 8
	v_mov_b32_e32 v1, s8
	v_readlane_b32 s100, v140, s14
	s_nop 1
	v_mov_b32_e32 v1, s100
	s_add_u32 s8, s38, s8
	s_addc_u32 s9, s39, 0
	v_cmp_lt_u32_e32 vcc, s89, v1
	v_mov_b32_e32 v1, 4
	s_cbranch_vccz .LBB0_731
	v_cmp_gt_i32_e32 vcc, 4, v1
	s_mov_b64 s[10:11], -1
	s_and_saveexec_b64 s[8:9], vcc
	s_cbranch_execnz .LBB0_734

; __device__ __forceinline__ int next_unit(unsigned* counters, int per_queue, LAS unsigned char* lds, int slot_off, const int wave) {
;     ...
;         for (unsigned k = 0; k < 8u; ++k) {
;             const unsigned q = (x + k) & 7u;
;             if (k > 0 && __hip_atomic_load(counters + q * 64, __ATOMIC_RELAXED, __HIP_MEMORY_SCOPE_AGENT) >= (unsigned)per_queue) continue;
;             const unsigned idx = __hip_atomic_fetch_add(counters + q * 64, 1u, __ATOMIC_RELAXED, __HIP_MEMORY_SCOPE_AGENT);
;             if (idx < (unsigned)per_queue) { res = (int)(q * (unsigned)per_queue + idx); break; }
;         }
;         slot[0] = res;
.LBB0_735:
	s_add_i32 s10, s0, 3
	s_and_b32 s16, s10, 7
	s_lshl_b32 s10, s16, 8
	v_mov_b32_e32 v1, s10
	v_readlane_b32 s100, v140, s16
	s_nop 1
	v_mov_b32_e32 v1, s100
	s_add_u32 s10, s38, s10
	s_addc_u32 s11, s39, 0
	v_cmp_lt_u32_e32 vcc, s89, v1
	v_mov_b32_e32 v1, 4
	s_cbranch_vccz .LBB0_738
	v_cmp_gt_i32_e32 vcc, 4, v1
	s_mov_b64 s[12:13], -1
	s_and_saveexec_b64 s[10:11], vcc
	s_cbranch_execnz .LBB0_741

; __device__ __forceinline__ int next_unit(unsigned* counters, int per_queue, LAS unsigned char* lds, int slot_off, const int wave) {
;     ...
;         for (unsigned k = 0; k < 8u; ++k) {
;             const unsigned q = (x + k) & 7u;
;             if (k > 0 && __hip_atomic_load(counters + q * 64, __ATOMIC_RELAXED, __HIP_MEMORY_SCOPE_AGENT) >= (unsigned)per_queue) continue;
;             const unsigned idx = __hip_atomic_fetch_add(counters + q * 64, 1u, __ATOMIC_RELAXED, __HIP_MEMORY_SCOPE_AGENT);
;             if (idx < (unsigned)per_queue) { res = (int)(q * (unsigned)per_queue + idx); break; }
;         }
;         slot[0] = res;
.LBB0_742:
	s_xor_b32 s1, s1, 4
	s_lshl_b32 s12, s1, 8
	v_mov_b32_e32 v1, s12
	v_readlane_b32 s100, v140, s1
	s_nop 1
	v_mov_b32_e32 v1, s100
	s_add_u32 s12, s38, s12
	s_addc_u32 s13, s39, 0
	v_cmp_lt_u32_e32 vcc, s89, v1
	v_mov_b32_e32 v1, 4
	s_cbranch_vccz .LBB0_745
	v_cmp_gt_i32_e32 vcc, 4, v1
	s_mov_b64 s[14:15], -1
	s_and_saveexec_b64 s[12:13], vcc
	s_cbranch_execnz .LBB0_748

; __device__ __forceinline__ int next_unit(unsigned* counters, int per_queue, LAS unsigned char* lds, int slot_off, const int wave) {
;     ...
;         for (unsigned k = 0; k < 8u; ++k) {
;             const unsigned q = (x + k) & 7u;
;             if (k > 0 && __hip_atomic_load(counters + q * 64, __ATOMIC_RELAXED, __HIP_MEMORY_SCOPE_AGENT) >= (unsigned)per_queue) continue;
;             const unsigned idx = __hip_atomic_fetch_add(counters + q * 64, 1u, __ATOMIC_RELAXED, __HIP_MEMORY_SCOPE_AGENT);
;             if (idx < (unsigned)per_queue) { res = (int)(q * (unsigned)per_queue + idx); break; }
;         }
;         slot[0] = res;
.LBB0_749:
	s_add_i32 s1, s0, 5
	s_and_b32 s1, s1, 7
	s_lshl_b32 s14, s1, 8
	v_mov_b32_e32 v1, s14
	v_readlane_b32 s100, v140, s1
	s_nop 1
	v_mov_b32_e32 v1, s100
	s_add_u32 s14, s38, s14
	s_addc_u32 s15, s39, 0
	v_cmp_lt_u32_e32 vcc, s89, v1
	v_mov_b32_e32 v1, 4
	s_cbranch_vccz .LBB0_752
	v_cmp_gt_i32_e32 vcc, 4, v1
	s_mov_b64 s[16:17], -1
	s_and_saveexec_b64 s[14:15], vcc
	s_cbranch_execnz .LBB0_755

; __device__ __forceinline__ int next_unit(unsigned* counters, int per_queue, LAS unsigned char* lds, int slot_off, const int wave) {
;     ...
;         for (unsigned k = 0; k < 8u; ++k) {
;             const unsigned q = (x + k) & 7u;
;             if (k > 0 && __hip_atomic_load(counters + q * 64, __ATOMIC_RELAXED, __HIP_MEMORY_SCOPE_AGENT) >= (unsigned)per_queue) continue;
;             const unsigned idx = __hip_atomic_fetch_add(counters + q * 64, 1u, __ATOMIC_RELAXED, __HIP_MEMORY_SCOPE_AGENT);
;             if (idx < (unsigned)per_queue) { res = (int)(q * (unsigned)per_queue + idx); break; }
;         }
;         slot[0] = res;
.LBB0_756:
	s_add_i32 s1, s0, 6
	s_and_b32 s1, s1, 7
	s_lshl_b32 s16, s1, 8
	v_mov_b32_e32 v1, s16
	v_readlane_b32 s100, v140, s1
	s_nop 1
	v_mov_b32_e32 v1, s100
	s_add_u32 s16, s38, s16
	s_addc_u32 s17, s39, 0
	v_cmp_lt_u32_e32 vcc, s89, v1
	v_mov_b32_e32 v1, 4
	s_cbranch_vccz .LBB0_759
	v_cmp_gt_i32_e32 vcc, 4, v1
	s_mov_b64 s[18:19], -1
	s_and_saveexec_b64 s[16:17], vcc
	s_cbranch_execnz .LBB0_762

; __device__ __forceinline__ int next_unit(unsigned* counters, int per_queue, LAS unsigned char* lds, int slot_off, const int wave) {
;     ...
;         for (unsigned k = 0; k < 8u; ++k) {
;             const unsigned q = (x + k) & 7u;
;             if (k > 0 && __hip_atomic_load(counters + q * 64, __ATOMIC_RELAXED, __HIP_MEMORY_SCOPE_AGENT) >= (unsigned)per_queue) continue;
;             const unsigned idx = __hip_atomic_fetch_add(counters + q * 64, 1u, __ATOMIC_RELAXED, __HIP_MEMORY_SCOPE_AGENT);
;             if (idx < (unsigned)per_queue) { res = (int)(q * (unsigned)per_queue + idx); break; }
;         }
;         slot[0] = res;
.LBB0_763:
	s_add_i32 s0, s0, -1
	s_and_b32 s0, s0, 7
	s_lshl_b32 s1, s0, 8
	v_mov_b32_e32 v1, s1
	v_readlane_b32 s100, v140, s0
	s_nop 1
	v_mov_b32_e32 v1, s100
	s_add_u32 s18, s38, s1
	s_addc_u32 s19, s39, 0
	v_cmp_lt_u32_e32 vcc, s89, v1
	s_cbranch_vccnz .LBB0_767
	s_mov_b64 s[22:23], exec
	v_mbcnt_lo_u32_b32 v1, s22, 0
	v_mbcnt_hi_u32_b32 v1, s23, v1
	v_cmp_eq_u32_e32 vcc, 0, v1
	s_and_saveexec_b64 s[20:21], vcc
	s_cbranch_execz .LBB0_766
	s_bcnt1_i32_b64 s1, s[22:23]
	v_mov_b32_e32 v2, s1
	global_atomic_add v2, v177, v2, s[18:19] sc0

; #define LAS __attribute__((address_space(3)))
; __device__ __forceinline__ int lane_id_v() { int l; asm volatile("v_mbcnt_lo_u32_b32 %0, -1, 0\n\tv_mbcnt_hi_u32_b32 %0, -1, %0" : "=v"(l)); return l & 63; }
; __device__ __forceinline__ int opaque_i(int x) { asm volatile("" : "+v"(x)); return x; }
; __device__ __forceinline__ int next_unit_pre(QPre& qp, unsigned* counters, int per_queue, LAS unsigned char* lds, int slot_off, const int wave) {
;     volatile LAS int* slot = (volatile LAS int*)(lds + opaque_i(slot_off));
;     const unsigned x = ((unsigned)__builtin_amdgcn_s_getreg((3 << 11) | 20)) & 7u;
;     qp.ctr = counters + x * 64;
;     if (wave == 0 && lane_id_v() == 0) {
;         int res = -1;
;         unsigned k0 = 0u;
;         if (qp.issued) { if (qp.pre < (unsigned)per_queue) res = (int)(x * (unsigned)per_queue + qp.pre); k0 = 1u; }
;         if (res < 0) {
;             for (unsigned k = k0; k < 8u; ++k) {
;                 const unsigned q = (x + k) & 7u;
;                 if (k > 0 && __hip_atomic_load(counters + q * 64, __ATOMIC_RELAXED, __HIP_MEMORY_SCOPE_AGENT) >= (unsigned)per_queue) continue;
;                 const unsigned idx = __hip_atomic_fetch_add(counters + q * 64, 1u, __ATOMIC_RELAXED, __HIP_MEMORY_SCOPE_AGENT);
;                 if (idx < (unsigned)per_queue) { res = (int)(q * (unsigned)per_queue + idx); break; }
;             }
;         }
;         slot[0] = res;
.LBB0_1595:
	s_nop 1
	v_mov_b32_e32 v0, 0x1fc00
	v_readlane_b32 s2, v254, 26
	s_getreg_b32 s1, hwreg(HW_REG_XCC_ID, 0, 4)
	v_readlane_b32 s3, v254, 27
	s_and_b64 vcc, exec, s[2:3]
	s_and_b32 s0, s1, 7
	s_cbranch_vccnz .LBB0_1611
	v_mbcnt_lo_u32_b32 v1, -1, 0
	v_mbcnt_hi_u32_b32 v1, -1, v1
	s_nop 0
	v_and_b32_e32 v1, 63, v1
	v_cmp_eq_u32_e32 vcc, 0, v1
	s_and_saveexec_b64 s[4:5], vcc
	s_cbranch_execz .LBB0_1610
	v_and_b32_e32 v1, 1, v103
	v_cmp_eq_u32_e32 vcc, 1, v1
	s_movk_i32 s2, 0xff
	v_cmp_lt_u32_e64 s[2:3], s2, v94
	v_lshl_add_u32 v1, s0, 8, v94
	s_xor_b64 s[8:9], vcc, -1
	s_or_b64 s[2:3], s[8:9], s[2:3]
	v_cmp_gt_i32_e32 vcc, 0, v1
	s_or_b64 s[8:9], s[2:3], vcc
	s_and_saveexec_b64 s[2:3], s[8:9]
	s_cbranch_execz .LBB0_1609
	v_and_b32_e32 v2, 0xff, v103
	v_mov_b32_e32 v1, -1
	s_mov_b64 s[16:17], 0
	s_mov_b64 s[98:99], exec
	s_mov_b64 exec, 0xff
	v_mbcnt_lo_u32_b32 v252, -1, 0
	v_lshlrev_b32_e32 v252, 8, v252
	global_load_dword v252, v252, s[6:7] sc1
	s_waitcnt vmcnt(0)
	s_mov_b64 exec, s[98:99]
	s_branch .LBB0_1600

; __device__ __forceinline__ int next_unit_pre(QPre& qp, unsigned* counters, int per_queue, LAS unsigned char* lds, int slot_off, const int wave) {
;     ...
;             for (unsigned k = k0; k < 8u; ++k) {
;                 const unsigned q = (x + k) & 7u;
;                 if (k > 0 && __hip_atomic_load(counters + q * 64, __ATOMIC_RELAXED, __HIP_MEMORY_SCOPE_AGENT) >= (unsigned)per_queue) continue;
;                 const unsigned idx = __hip_atomic_fetch_add(counters + q * 64, 1u, __ATOMIC_RELAXED, __HIP_MEMORY_SCOPE_AGENT);
;                 if (idx < (unsigned)per_queue) { res = (int)(q * (unsigned)per_queue + idx); break; }
.LBB0_1600:
	v_add_u32_e32 v3, s1, v2
	v_and_b32_e32 v3, 7, v3
	v_lshlrev_b32_e32 v4, 6, v3
	v_cmp_eq_u32_e64 s[18:19], 0, v2
	v_cmp_ne_u32_e32 vcc, 0, v2
	v_lshlrev_b32_e32 v4, 2, v4
	s_and_saveexec_b64 s[20:21], vcc
	s_cbranch_execz .LBB0_1602
	v_readfirstlane_b32 s101, v3
	s_nop 3
	v_readlane_b32 s100, v252, s101
	s_nop 1
	v_mov_b32_e32 v5, s100
	s_andn2_b64 s[8:9], s[18:19], exec
	v_cmp_gt_u32_e32 vcc, s74, v5
	s_and_b64 s[10:11], vcc, exec
	s_or_b64 s[18:19], s[8:9], s[10:11]

; __device__ __forceinline__ int next_unit_pre(QPre& qp, unsigned* counters, int per_queue, LAS unsigned char* lds, int slot_off, const int wave) {
;     ...
;         if (qp.issued) { if (qp.pre < (unsigned)per_queue) res = (int)(x * (unsigned)per_queue + qp.pre); k0 = 1u; }
;         if (res < 0) {
;             for (unsigned k = k0; k < 8u; ++k) {
;                 const unsigned q = (x + k) & 7u;
;                 if (k > 0 && __hip_atomic_load(counters + q * 64, __ATOMIC_RELAXED, __HIP_MEMORY_SCOPE_AGENT) >= (unsigned)per_queue) continue;
;                 const unsigned idx = __hip_atomic_fetch_add(counters + q * 64, 1u, __ATOMIC_RELAXED, __HIP_MEMORY_SCOPE_AGENT);
;                 if (idx < (unsigned)per_queue) { res = (int)(q * (unsigned)per_queue + idx); break; }
;             }
.LBB0_2376:
	s_or_b64 exec, exec, s[4:5]
	s_waitcnt vmcnt(0)
	v_readfirstlane_b32 s4, v3
	s_nop 1
	v_add_u32_e32 v2, s4, v2
	s_movk_i32 s4, 0x7f
	v_cmp_lt_u32_e32 vcc, s4, v2
	v_lshl_add_u32 v2, s1, 7, v2
	s_and_saveexec_b64 s[4:5], vcc
	s_cbranch_execz .LBB0_2429
	s_mov_b64 s[98:99], exec
	s_mov_b64 exec, 0xff
	v_mbcnt_lo_u32_b32 v252, -1, 0
	v_lshlrev_b32_e32 v252, 8, v252
	v_readlane_b32 s100, v254, 31
	v_readlane_b32 s101, v254, 32
	s_nop 4
	global_load_dword v252, v252, s[100:101] sc1
	s_waitcnt vmcnt(0)
	s_mov_b64 exec, s[98:99]
	s_add_i32 s6, s0, 1
	s_and_b32 s12, s6, 7
	s_lshl_b32 s6, s12, 8
	v_readlane_b32 s8, v254, 31
	v_mov_b32_e32 v2, s6
	v_readlane_b32 s9, v254, 32
	s_add_u32 s6, s8, s6
	s_addc_u32 s7, s9, 0
	s_nop 2
	v_readlane_b32 s100, v252, s12
	s_nop 1
	v_mov_b32_e32 v2, s100
	s_movk_i32 s8, 0x7f
	v_cmp_lt_u32_e32 vcc, s8, v2
	s_cbranch_vccnz .LBB0_2381
	s_mov_b64 s[10:11], exec
	v_mbcnt_lo_u32_b32 v2, s10, 0
	v_mbcnt_hi_u32_b32 v2, s11, v2
	v_cmp_eq_u32_e32 vcc, 0, v2
	s_and_saveexec_b64 s[8:9], vcc
	s_cbranch_execz .LBB0_2380
	s_bcnt1_i32_b64 s10, s[10:11]
	v_mov_b32_e32 v3, s10
	global_atomic_add v3, v145, v3, s[6:7] sc0

; __device__ __forceinline__ int next_unit_pre(QPre& qp, unsigned* counters, int per_queue, LAS unsigned char* lds, int slot_off, const int wave) {
;     ...
;             for (unsigned k = k0; k < 8u; ++k) {
;                 const unsigned q = (x + k) & 7u;
;                 if (k > 0 && __hip_atomic_load(counters + q * 64, __ATOMIC_RELAXED, __HIP_MEMORY_SCOPE_AGENT) >= (unsigned)per_queue) continue;
;                 const unsigned idx = __hip_atomic_fetch_add(counters + q * 64, 1u, __ATOMIC_RELAXED, __HIP_MEMORY_SCOPE_AGENT);
;                 if (idx < (unsigned)per_queue) { res = (int)(q * (unsigned)per_queue + idx); break; }
.LBB0_2383:
	s_or_b64 exec, exec, s[6:7]
	s_and_saveexec_b64 s[6:7], s[8:9]
	s_cbranch_execz .LBB0_2428
	s_add_i32 s8, s0, 2
	s_and_b32 s14, s8, 7
	s_lshl_b32 s8, s14, 8
	v_readlane_b32 s10, v254, 31
	v_mov_b32_e32 v3, s8
	v_readlane_b32 s11, v254, 32
	s_add_u32 s8, s10, s8
	s_addc_u32 s9, s11, 0
	s_nop 2
	v_readlane_b32 s100, v252, s14
	s_nop 1
	v_mov_b32_e32 v3, s100
	s_movk_i32 s10, 0x7f
	v_cmp_lt_u32_e32 vcc, s10, v3
	v_mov_b32_e32 v3, 4
	s_cbranch_vccz .LBB0_2387
	v_cmp_gt_i32_e32 vcc, 4, v3
	s_mov_b64 s[10:11], -1
	s_and_saveexec_b64 s[8:9], vcc
	s_cbranch_execnz .LBB0_2390

; __device__ __forceinline__ int next_unit_pre(QPre& qp, unsigned* counters, int per_queue, LAS unsigned char* lds, int slot_off, const int wave) {
;     ...
;             for (unsigned k = k0; k < 8u; ++k) {
;                 const unsigned q = (x + k) & 7u;
;                 if (k > 0 && __hip_atomic_load(counters + q * 64, __ATOMIC_RELAXED, __HIP_MEMORY_SCOPE_AGENT) >= (unsigned)per_queue) continue;
;                 const unsigned idx = __hip_atomic_fetch_add(counters + q * 64, 1u, __ATOMIC_RELAXED, __HIP_MEMORY_SCOPE_AGENT);
;                 if (idx < (unsigned)per_queue) { res = (int)(q * (unsigned)per_queue + idx); break; }
.LBB0_2391:
	s_add_i32 s10, s0, 3
	s_and_b32 s16, s10, 7
	s_lshl_b32 s10, s16, 8
	v_readlane_b32 s12, v254, 31
	v_mov_b32_e32 v3, s10
	v_readlane_b32 s13, v254, 32
	s_add_u32 s10, s12, s10
	s_addc_u32 s11, s13, 0
	s_nop 2
	v_readlane_b32 s100, v252, s16
	s_nop 1
	v_mov_b32_e32 v3, s100
	s_movk_i32 s12, 0x7f
	v_cmp_lt_u32_e32 vcc, s12, v3
	v_mov_b32_e32 v3, 4
	s_cbranch_vccz .LBB0_2394
	v_cmp_gt_i32_e32 vcc, 4, v3
	s_mov_b64 s[12:13], -1
	s_and_saveexec_b64 s[10:11], vcc
	s_cbranch_execnz .LBB0_2397

; __device__ __forceinline__ int next_unit_pre(QPre& qp, unsigned* counters, int per_queue, LAS unsigned char* lds, int slot_off, const int wave) {
;     ...
;             for (unsigned k = k0; k < 8u; ++k) {
;                 const unsigned q = (x + k) & 7u;
;                 if (k > 0 && __hip_atomic_load(counters + q * 64, __ATOMIC_RELAXED, __HIP_MEMORY_SCOPE_AGENT) >= (unsigned)per_queue) continue;
;                 const unsigned idx = __hip_atomic_fetch_add(counters + q * 64, 1u, __ATOMIC_RELAXED, __HIP_MEMORY_SCOPE_AGENT);
;                 if (idx < (unsigned)per_queue) { res = (int)(q * (unsigned)per_queue + idx); break; }
.LBB0_2398:
	s_xor_b32 s1, s1, 4
	s_lshl_b32 s12, s1, 8
	v_readlane_b32 s14, v254, 31
	v_mov_b32_e32 v3, s12
	v_readlane_b32 s15, v254, 32
	s_add_u32 s12, s14, s12
	s_addc_u32 s13, s15, 0
	s_nop 2
	v_readlane_b32 s100, v252, s1
	s_nop 1
	v_mov_b32_e32 v3, s100
	s_movk_i32 s14, 0x7f
	v_cmp_lt_u32_e32 vcc, s14, v3
	v_mov_b32_e32 v3, 4
	s_cbranch_vccz .LBB0_2401
	v_cmp_gt_i32_e32 vcc, 4, v3
	s_mov_b64 s[14:15], -1
	s_and_saveexec_b64 s[12:13], vcc
	s_cbranch_execnz .LBB0_2404

; __device__ __forceinline__ int next_unit_pre(QPre& qp, unsigned* counters, int per_queue, LAS unsigned char* lds, int slot_off, const int wave) {
;     ...
;             for (unsigned k = k0; k < 8u; ++k) {
;                 const unsigned q = (x + k) & 7u;
;                 if (k > 0 && __hip_atomic_load(counters + q * 64, __ATOMIC_RELAXED, __HIP_MEMORY_SCOPE_AGENT) >= (unsigned)per_queue) continue;
;                 const unsigned idx = __hip_atomic_fetch_add(counters + q * 64, 1u, __ATOMIC_RELAXED, __HIP_MEMORY_SCOPE_AGENT);
;                 if (idx < (unsigned)per_queue) { res = (int)(q * (unsigned)per_queue + idx); break; }
.LBB0_2405:
	s_add_i32 s1, s0, 5
	s_and_b32 s1, s1, 7
	s_lshl_b32 s14, s1, 8
	v_readlane_b32 s16, v254, 31
	v_mov_b32_e32 v3, s14
	v_readlane_b32 s17, v254, 32
	s_add_u32 s14, s16, s14
	s_addc_u32 s15, s17, 0
	s_nop 2
	v_readlane_b32 s100, v252, s1
	s_nop 1
	v_mov_b32_e32 v3, s100
	s_movk_i32 s16, 0x7f
	v_cmp_lt_u32_e32 vcc, s16, v3
	v_mov_b32_e32 v3, 4
	s_cbranch_vccz .LBB0_2408
	v_cmp_gt_i32_e32 vcc, 4, v3
	s_mov_b64 s[16:17], -1
	s_and_saveexec_b64 s[14:15], vcc
	s_cbranch_execnz .LBB0_2411

; __device__ __forceinline__ int next_unit_pre(QPre& qp, unsigned* counters, int per_queue, LAS unsigned char* lds, int slot_off, const int wave) {
;     ...
;             for (unsigned k = k0; k < 8u; ++k) {
;                 const unsigned q = (x + k) & 7u;
;                 if (k > 0 && __hip_atomic_load(counters + q * 64, __ATOMIC_RELAXED, __HIP_MEMORY_SCOPE_AGENT) >= (unsigned)per_queue) continue;
;                 const unsigned idx = __hip_atomic_fetch_add(counters + q * 64, 1u, __ATOMIC_RELAXED, __HIP_MEMORY_SCOPE_AGENT);
;                 if (idx < (unsigned)per_queue) { res = (int)(q * (unsigned)per_queue + idx); break; }
.LBB0_2412:
	s_add_i32 s1, s0, 6
	s_and_b32 s1, s1, 7
	s_lshl_b32 s16, s1, 8
	v_readlane_b32 s18, v254, 31
	v_mov_b32_e32 v3, s16
	v_readlane_b32 s19, v254, 32
	s_add_u32 s16, s18, s16
	s_addc_u32 s17, s19, 0
	s_nop 2
	v_readlane_b32 s100, v252, s1
	s_nop 1
	v_mov_b32_e32 v3, s100
	s_movk_i32 s18, 0x7f
	v_cmp_lt_u32_e32 vcc, s18, v3
	v_mov_b32_e32 v3, 4
	s_cbranch_vccz .LBB0_2415
	v_cmp_gt_i32_e32 vcc, 4, v3
	s_mov_b64 s[18:19], -1
	s_and_saveexec_b64 s[16:17], vcc
	s_cbranch_execnz .LBB0_2418

; __device__ __forceinline__ int next_unit_pre(QPre& qp, unsigned* counters, int per_queue, LAS unsigned char* lds, int slot_off, const int wave) {
;     ...
;             for (unsigned k = k0; k < 8u; ++k) {
;                 const unsigned q = (x + k) & 7u;
;                 if (k > 0 && __hip_atomic_load(counters + q * 64, __ATOMIC_RELAXED, __HIP_MEMORY_SCOPE_AGENT) >= (unsigned)per_queue) continue;
;                 const unsigned idx = __hip_atomic_fetch_add(counters + q * 64, 1u, __ATOMIC_RELAXED, __HIP_MEMORY_SCOPE_AGENT);
;                 if (idx < (unsigned)per_queue) { res = (int)(q * (unsigned)per_queue + idx); break; }
.LBB0_2419:
	s_add_i32 s0, s0, -1
	s_and_b32 s0, s0, 7
	s_lshl_b32 s1, s0, 8
	v_readlane_b32 s18, v254, 31
	v_mov_b32_e32 v3, s1
	v_readlane_b32 s19, v254, 32
	s_nop 4
	v_readlane_b32 s100, v252, s0
	s_nop 1
	v_mov_b32_e32 v3, s100
	s_add_u32 s18, s18, s1
	s_movk_i32 s1, 0x7f
	s_addc_u32 s19, s19, 0
	v_cmp_lt_u32_e32 vcc, s1, v3
	s_cbranch_vccnz .LBB0_2423
	s_mov_b64 s[22:23], exec
	v_mbcnt_lo_u32_b32 v3, s22, 0
	v_mbcnt_hi_u32_b32 v3, s23, v3
	v_cmp_eq_u32_e32 vcc, 0, v3
	s_and_saveexec_b64 s[20:21], vcc
	s_cbranch_execz .LBB0_2422
	s_bcnt1_i32_b64 s1, s[22:23]
	v_mov_b32_e32 v4, s1
	global_atomic_add v4, v145, v4, s[18:19] sc0

; #define LAS __attribute__((address_space(3)))
; __device__ __forceinline__ int lane_id_v() { int l; asm volatile("v_mbcnt_lo_u32_b32 %0, -1, 0\n\tv_mbcnt_hi_u32_b32 %0, -1, %0" : "=v"(l)); return l & 63; }
; __device__ __forceinline__ int opaque_i(int x) { asm volatile("" : "+v"(x)); return x; }
; __device__ __forceinline__ int next_unit_pre(QPre& qp, unsigned* counters, int per_queue, LAS unsigned char* lds, int slot_off, const int wave) {
;     volatile LAS int* slot = (volatile LAS int*)(lds + opaque_i(slot_off));
;     const unsigned x = ((unsigned)__builtin_amdgcn_s_getreg((3 << 11) | 20)) & 7u;
;     qp.ctr = counters + x * 64;
;     if (wave == 0 && lane_id_v() == 0) {
;         int res = -1;
;         unsigned k0 = 0u;
;         if (qp.issued) { if (qp.pre < (unsigned)per_queue) res = (int)(x * (unsigned)per_queue + qp.pre); k0 = 1u; }
;         if (res < 0) {
;             for (unsigned k = k0; k < 8u; ++k) {
;                 const unsigned q = (x + k) & 7u;
;                 if (k > 0 && __hip_atomic_load(counters + q * 64, __ATOMIC_RELAXED, __HIP_MEMORY_SCOPE_AGENT) >= (unsigned)per_queue) continue;
;                 const unsigned idx = __hip_atomic_fetch_add(counters + q * 64, 1u, __ATOMIC_RELAXED, __HIP_MEMORY_SCOPE_AGENT);
;                 if (idx < (unsigned)per_queue) { res = (int)(q * (unsigned)per_queue + idx); break; }
;             }
;         }
;         slot[0] = res;
.LBB0_2502:
	v_mov_b32_e32 v0, 0x1fc00
	v_readlane_b32 s4, v254, 26
	s_getreg_b32 s1, hwreg(HW_REG_XCC_ID, 0, 4)
	v_readlane_b32 s5, v254, 27
	s_and_b64 vcc, exec, s[4:5]
	s_and_b32 s0, s1, 7
	s_cbranch_vccnz .LBB0_2518
	v_mbcnt_lo_u32_b32 v2, -1, 0
	v_mbcnt_hi_u32_b32 v2, -1, v2
	s_nop 0
	v_and_b32_e32 v2, 63, v2
	v_cmp_eq_u32_e32 vcc, 0, v2
	s_and_saveexec_b64 s[6:7], vcc
	s_cbranch_execz .LBB0_2517
	v_and_b32_e32 v2, 1, v154
	v_cmp_eq_u32_e32 vcc, 1, v2
	s_movk_i32 s4, 0xff
	v_cmp_lt_u32_e64 s[4:5], s4, v142
	v_lshl_add_u32 v2, s0, 8, v142
	s_xor_b64 s[8:9], vcc, -1
	s_or_b64 s[4:5], s[8:9], s[4:5]
	v_cmp_gt_i32_e32 vcc, 0, v2
	s_or_b64 s[8:9], s[4:5], vcc
	s_and_saveexec_b64 s[4:5], s[8:9]
	s_cbranch_execz .LBB0_2516
	v_and_b32_e32 v3, 0xff, v154
	v_mov_b32_e32 v2, -1
	s_mov_b64 s[8:9], 0
	s_mov_b64 s[98:99], exec
	s_mov_b64 exec, 0xff
	v_mbcnt_lo_u32_b32 v253, -1, 0
	v_lshlrev_b32_e32 v253, 8, v253
	global_load_dword v253, v253, s[38:39] sc1
	s_waitcnt vmcnt(0)
	s_mov_b64 exec, s[98:99]
	s_branch .LBB0_2507

; __device__ __forceinline__ int next_unit_pre(QPre& qp, unsigned* counters, int per_queue, LAS unsigned char* lds, int slot_off, const int wave) {
;     ...
;             for (unsigned k = k0; k < 8u; ++k) {
;                 const unsigned q = (x + k) & 7u;
;                 if (k > 0 && __hip_atomic_load(counters + q * 64, __ATOMIC_RELAXED, __HIP_MEMORY_SCOPE_AGENT) >= (unsigned)per_queue) continue;
;                 const unsigned idx = __hip_atomic_fetch_add(counters + q * 64, 1u, __ATOMIC_RELAXED, __HIP_MEMORY_SCOPE_AGENT);
;                 if (idx < (unsigned)per_queue) { res = (int)(q * (unsigned)per_queue + idx); break; }
.LBB0_2507:
	v_add_u32_e32 v4, s1, v3
	v_and_b32_e32 v4, 7, v4
	v_lshlrev_b32_e32 v5, 6, v4
	v_cmp_eq_u32_e64 s[10:11], 0, v3
	v_cmp_ne_u32_e32 vcc, 0, v3
	v_lshlrev_b32_e32 v5, 2, v5
	s_and_saveexec_b64 s[12:13], vcc
	s_cbranch_execz .LBB0_2509
	v_readfirstlane_b32 s101, v4
	s_nop 3
	v_readlane_b32 s100, v253, s101
	s_nop 1
	v_mov_b32_e32 v6, s100
	s_andn2_b64 s[10:11], s[10:11], exec
	v_cmp_gt_u32_e32 vcc, s81, v6
	s_and_b64 s[14:15], vcc, exec
	s_or_b64 s[10:11], s[10:11], s[14:15]
